# as v67 plus MoE-up SwiGLU fp8 epilogue with operand scales folded into constants (bit-identical f32 math, 2 fewer VALU ops per element, no packed f32 mul)
# speedup vs baseline: 1.0052x; 1.0052x over previous
.LBB0_1960:
	s_nop 15
	s_nop 15
	s_nop 15
	v_lshl_add_u32 v6, s61, 8, v173
	v_mul_f32_e32 v4, 0xb9b8aa3b, v158
	v_exp_f32_e32 v10, v4
	v_mul_f32_e32 v11, 0xb9b8aa3b, v159
	v_exp_f32_e32 v13, v11
	v_add_f32_e32 v10, 1.0, v10
	v_rcp_f32_e32 v10, v10
	v_lshl_or_b32 v2, s60, 7, v193
	v_mov_b64_e32 v[4:5], s[8:9]
	v_ashrrev_i32_e32 v3, 31, v2
	v_mul_f32_e32 v11, v158, v10
	v_add_f32_e32 v7, 1.0, v13
	v_rcp_f32_e32 v7, v7
	v_mul_f32_e32 v14, 0xb9b8aa3b, v160
	v_exp_f32_e32 v14, v14
	v_mad_i64_i32 v[8:9], s[22:23], v6, s46, v[4:5]
	v_mul_f32_e32 v15, v154, v11
	v_mul_f32_e32 v15, 0x35000000, v15
	v_mul_f32_e32 v11, v159, v7
	v_add_f32_e32 v7, 1.0, v14
	v_mul_f32_e32 v14, 0xb9b8aa3b, v161
	v_rcp_f32_e32 v7, v7
	v_exp_f32_e32 v14, v14
	v_lshl_add_u64 v[8:9], v[8:9], 0, v[2:3]
	v_mul_f32_e32 v16, v155, v11
	v_mul_f32_e32 v16, 0x35000000, v16
	v_mul_f32_e32 v11, v160, v7
	v_add_f32_e32 v7, 1.0, v14
	v_rcp_f32_e32 v7, v7
	s_andn2_b64 vcc, exec, s[4:5]
	v_mul_f32_e32 v13, v156, v11
	v_mul_f32_e32 v13, 0x35000000, v13
	v_mul_f32_e32 v11, v161, v7
	v_mul_f32_e32 v10, 0xb9b8aa3b, v150
	v_exp_f32_e32 v12, v10
	v_med3_f32 v13, v13, s47, v197
	v_mul_f32_e32 v14, v157, v11
	v_mul_f32_e32 v14, 0x35000000, v14
	v_add_f32_e32 v10, 1.0, v12
	v_mul_f32_e32 v11, 0xb9b8aa3b, v151
	v_rcp_f32_e32 v10, v10
	v_exp_f32_e32 v17, v11
	v_med3_f32 v14, v14, s47, v197
	s_mov_b64 s[4:5], -1
	v_mul_f32_e32 v11, v150, v10
	v_add_f32_e32 v7, 1.0, v17
	v_rcp_f32_e32 v7, v7
	v_mul_f32_e32 v18, 0xb9b8aa3b, v152
	v_exp_f32_e32 v18, v18
	s_nop 0
	v_mul_f32_e32 v19, v146, v11
	v_mul_f32_e32 v19, 0x35000000, v19
	v_mul_f32_e32 v11, v151, v7
	v_add_f32_e32 v7, 1.0, v18
	v_mul_f32_e32 v18, 0xb9b8aa3b, v153
	v_rcp_f32_e32 v7, v7
	v_exp_f32_e32 v18, v18
	s_nop 0
	v_mul_f32_e32 v20, v147, v11
	v_mul_f32_e32 v20, 0x35000000, v20
	v_mul_f32_e32 v11, v152, v7
	v_add_f32_e32 v7, 1.0, v18
	v_rcp_f32_e32 v7, v7
	s_nop 0
	v_mul_f32_e32 v17, v148, v11
	v_mul_f32_e32 v17, 0x35000000, v17
	v_mul_f32_e32 v11, v153, v7
	v_med3_f32 v12, v16, s47, v197
	v_mul_f32_e32 v7, v149, v11
	v_mul_f32_e32 v7, 0x35000000, v7
	v_med3_f32 v11, v15, s47, v197
	v_mov_b32_e32 v10, v169
	v_cvt_pk_fp8_f32 v10, v11, v12
	v_med3_f32 v12, v19, s47, v197
	v_med3_f32 v15, v20, s47, v197
	v_mov_b32_e32 v11, v169
	v_cvt_pk_fp8_f32 v11, v12, v15
	v_med3_f32 v12, v17, s47, v197
	v_med3_f32 v7, v7, s47, v197
	v_cvt_pk_fp8_f32 v10, v13, v14 op_sel:[0,0,1]
	v_cvt_pk_fp8_f32 v11, v12, v7 op_sel:[0,0,1]
	v_mul_f32_e32 v12, 0xb9b8aa3b, v142
	v_exp_f32_e32 v12, v12
	global_store_dwordx2 v[8:9], v[10:11], off
	v_mul_f32_e32 v9, 0xb9b8aa3b, v143
	v_add_f32_e32 v8, 1.0, v12
	v_rcp_f32_e32 v8, v8
	v_exp_f32_e32 v12, v9
	v_or_b32_e32 v10, 16, v6
	v_mul_f32_e32 v9, v142, v8
	v_add_f32_e32 v7, 1.0, v12
	v_rcp_f32_e32 v7, v7
	v_mul_f32_e32 v13, 0xb9b8aa3b, v144
	v_exp_f32_e32 v13, v13
	s_nop 0
	v_mul_f32_e32 v14, v138, v9
	v_mul_f32_e32 v14, 0x35000000, v14
	v_mul_f32_e32 v9, v143, v7
	v_add_f32_e32 v7, 1.0, v13
	v_mul_f32_e32 v13, 0xb9b8aa3b, v145
	v_rcp_f32_e32 v7, v7
	v_exp_f32_e32 v13, v13
	s_nop 0
	v_mul_f32_e32 v15, v139, v9
	v_mul_f32_e32 v15, 0x35000000, v15
	v_mul_f32_e32 v9, v144, v7
	v_add_f32_e32 v7, 1.0, v13
	v_rcp_f32_e32 v7, v7
	s_nop 0
	v_mul_f32_e32 v12, v140, v9
	v_mul_f32_e32 v12, 0x35000000, v12
	v_mul_f32_e32 v9, v145, v7
	v_mul_f32_e32 v8, 0xb9b8aa3b, v134
	v_exp_f32_e32 v11, v8
	v_med3_f32 v12, v12, s47, v197
	v_mul_f32_e32 v13, v141, v9
	v_mul_f32_e32 v13, 0x35000000, v13
	v_add_f32_e32 v8, 1.0, v11
	v_mul_f32_e32 v9, 0xb9b8aa3b, v135
	v_rcp_f32_e32 v8, v8
	v_exp_f32_e32 v16, v9
	v_med3_f32 v13, v13, s47, v197
	v_mul_f32_e32 v9, v134, v8
	v_add_f32_e32 v7, 1.0, v16
	v_rcp_f32_e32 v7, v7
	v_mul_f32_e32 v17, 0xb9b8aa3b, v136
	v_exp_f32_e32 v17, v17
	s_nop 0
	v_mul_f32_e32 v18, v130, v9
	v_mul_f32_e32 v18, 0x35000000, v18
	v_mul_f32_e32 v9, v135, v7
	v_add_f32_e32 v7, 1.0, v17
	v_mul_f32_e32 v17, 0xb9b8aa3b, v137
	v_rcp_f32_e32 v7, v7
	v_exp_f32_e32 v17, v17
	s_nop 0
	v_mul_f32_e32 v19, v131, v9
	v_mul_f32_e32 v19, 0x35000000, v19
	v_mul_f32_e32 v9, v136, v7
	v_add_f32_e32 v7, 1.0, v17
	v_rcp_f32_e32 v7, v7
	s_nop 0
	v_mul_f32_e32 v16, v132, v9
	v_mul_f32_e32 v16, 0x35000000, v16
	v_mul_f32_e32 v9, v137, v7
	v_med3_f32 v11, v15, s47, v197
	v_mul_f32_e32 v7, v133, v9
	v_mul_f32_e32 v7, 0x35000000, v7
	v_med3_f32 v9, v14, s47, v197
	v_mov_b32_e32 v8, v169
	v_cvt_pk_fp8_f32 v8, v9, v11
	v_med3_f32 v11, v18, s47, v197
	v_med3_f32 v14, v19, s47, v197
	v_mov_b32_e32 v9, v169
	v_cvt_pk_fp8_f32 v9, v11, v14
	v_med3_f32 v11, v16, s47, v197
	v_med3_f32 v7, v7, s47, v197
	v_cvt_pk_fp8_f32 v8, v12, v13 op_sel:[0,0,1]
	v_cvt_pk_fp8_f32 v9, v11, v7 op_sel:[0,0,1]
	v_mad_i64_i32 v[10:11], s[22:23], v10, s46, v[4:5]
	v_lshl_add_u64 v[10:11], v[10:11], 0, v[2:3]
	global_store_dwordx2 v[10:11], v[8:9], off
	v_mul_f32_e32 v8, 0xb9b8aa3b, v126
	v_exp_f32_e32 v10, v8
	v_mul_f32_e32 v11, 0xb9b8aa3b, v127
	v_exp_f32_e32 v13, v11
	v_add_f32_e32 v10, 1.0, v10
	v_rcp_f32_e32 v10, v10
	v_or_b32_e32 v8, 32, v6
	v_mad_i64_i32 v[8:9], s[22:23], v8, s46, v[4:5]
	v_mul_f32_e32 v11, v126, v10
	v_add_f32_e32 v7, 1.0, v13
	v_rcp_f32_e32 v7, v7
	v_mul_f32_e32 v14, 0xb9b8aa3b, v128
	v_exp_f32_e32 v14, v14
	v_lshl_add_u64 v[8:9], v[8:9], 0, v[2:3]
	v_mul_f32_e32 v15, v122, v11
	v_mul_f32_e32 v15, 0x35000000, v15
	v_mul_f32_e32 v11, v127, v7
	v_add_f32_e32 v7, 1.0, v14
	v_mul_f32_e32 v14, 0xb9b8aa3b, v129
	v_rcp_f32_e32 v7, v7
	v_exp_f32_e32 v14, v14
	s_nop 0
	v_mul_f32_e32 v16, v123, v11
	v_mul_f32_e32 v16, 0x35000000, v16
	v_mul_f32_e32 v11, v128, v7
	v_add_f32_e32 v7, 1.0, v14
	v_rcp_f32_e32 v7, v7
	s_nop 0
	v_mul_f32_e32 v13, v124, v11
	v_mul_f32_e32 v13, 0x35000000, v13
	v_mul_f32_e32 v11, v129, v7
	v_mul_f32_e32 v10, 0xb9b8aa3b, v118
	v_exp_f32_e32 v12, v10
	v_med3_f32 v13, v13, s47, v197
	v_mul_f32_e32 v14, v125, v11
	v_mul_f32_e32 v14, 0x35000000, v14
	v_add_f32_e32 v10, 1.0, v12
	v_mul_f32_e32 v11, 0xb9b8aa3b, v119
	v_rcp_f32_e32 v10, v10
	v_exp_f32_e32 v17, v11
	v_med3_f32 v14, v14, s47, v197
	v_mul_f32_e32 v11, v118, v10
	v_add_f32_e32 v7, 1.0, v17
	v_rcp_f32_e32 v7, v7
	v_mul_f32_e32 v18, 0xb9b8aa3b, v120
	v_exp_f32_e32 v18, v18
	s_nop 0
	v_mul_f32_e32 v19, v114, v11
	v_mul_f32_e32 v19, 0x35000000, v19
	v_mul_f32_e32 v11, v119, v7
	v_add_f32_e32 v7, 1.0, v18
	v_mul_f32_e32 v18, 0xb9b8aa3b, v121
	v_rcp_f32_e32 v7, v7
	v_exp_f32_e32 v18, v18
	s_nop 0
	v_mul_f32_e32 v20, v115, v11
	v_mul_f32_e32 v20, 0x35000000, v20
	v_mul_f32_e32 v11, v120, v7
	v_add_f32_e32 v7, 1.0, v18
	v_rcp_f32_e32 v7, v7
	s_nop 0
	v_mul_f32_e32 v17, v116, v11
	v_mul_f32_e32 v17, 0x35000000, v17
	v_mul_f32_e32 v11, v121, v7
	v_med3_f32 v12, v16, s47, v197
	v_mul_f32_e32 v7, v117, v11
	v_mul_f32_e32 v7, 0x35000000, v7
	v_med3_f32 v11, v15, s47, v197
	v_mov_b32_e32 v10, v169
	v_cvt_pk_fp8_f32 v10, v11, v12
	v_med3_f32 v12, v19, s47, v197
	v_med3_f32 v15, v20, s47, v197
	v_mov_b32_e32 v11, v169
	v_cvt_pk_fp8_f32 v11, v12, v15
	v_med3_f32 v12, v17, s47, v197
	v_med3_f32 v7, v7, s47, v197
	v_cvt_pk_fp8_f32 v10, v13, v14 op_sel:[0,0,1]
	v_cvt_pk_fp8_f32 v11, v12, v7 op_sel:[0,0,1]
	v_mul_f32_e32 v12, 0xb9b8aa3b, v110
	v_exp_f32_e32 v12, v12
	global_store_dwordx2 v[8:9], v[10:11], off
	v_mul_f32_e32 v9, 0xb9b8aa3b, v111
	v_add_f32_e32 v8, 1.0, v12
	v_rcp_f32_e32 v8, v8
	v_exp_f32_e32 v12, v9
	v_or_b32_e32 v10, 48, v6
	v_mul_f32_e32 v9, v110, v8
	v_add_f32_e32 v7, 1.0, v12
	v_rcp_f32_e32 v7, v7
	v_mul_f32_e32 v13, 0xb9b8aa3b, v112
	v_exp_f32_e32 v13, v13
	s_nop 0
	v_mul_f32_e32 v14, v106, v9
	v_mul_f32_e32 v14, 0x35000000, v14
	v_mul_f32_e32 v9, v111, v7
	v_add_f32_e32 v7, 1.0, v13
	v_mul_f32_e32 v13, 0xb9b8aa3b, v113
	v_rcp_f32_e32 v7, v7
	v_exp_f32_e32 v13, v13
	s_nop 0
	v_mul_f32_e32 v15, v107, v9
	v_mul_f32_e32 v15, 0x35000000, v15
	v_mul_f32_e32 v9, v112, v7
	v_add_f32_e32 v7, 1.0, v13
	v_rcp_f32_e32 v7, v7
	s_nop 0
	v_mul_f32_e32 v12, v108, v9
	v_mul_f32_e32 v12, 0x35000000, v12
	v_mul_f32_e32 v9, v113, v7
	v_mul_f32_e32 v8, 0xb9b8aa3b, v102
	v_exp_f32_e32 v11, v8
	v_med3_f32 v12, v12, s47, v197
	v_mul_f32_e32 v13, v109, v9
	v_mul_f32_e32 v13, 0x35000000, v13
	v_add_f32_e32 v8, 1.0, v11
	v_mul_f32_e32 v9, 0xb9b8aa3b, v103
	v_rcp_f32_e32 v8, v8
	v_exp_f32_e32 v16, v9
	v_med3_f32 v13, v13, s47, v197
	v_mul_f32_e32 v9, v102, v8
	v_add_f32_e32 v7, 1.0, v16
	v_rcp_f32_e32 v7, v7
	v_mul_f32_e32 v17, 0xb9b8aa3b, v104
	v_exp_f32_e32 v17, v17
	s_nop 0
	v_mul_f32_e32 v18, v98, v9
	v_mul_f32_e32 v18, 0x35000000, v18
	v_mul_f32_e32 v9, v103, v7
	v_add_f32_e32 v7, 1.0, v17
	v_mul_f32_e32 v17, 0xb9b8aa3b, v105
	v_rcp_f32_e32 v7, v7
	v_exp_f32_e32 v17, v17
	s_nop 0
	v_mul_f32_e32 v19, v99, v9
	v_mul_f32_e32 v19, 0x35000000, v19
	v_mul_f32_e32 v9, v104, v7
	v_add_f32_e32 v7, 1.0, v17
	v_rcp_f32_e32 v7, v7
	s_nop 0
	v_mul_f32_e32 v16, v100, v9
	v_mul_f32_e32 v16, 0x35000000, v16
	v_mul_f32_e32 v9, v105, v7
	v_med3_f32 v11, v15, s47, v197
	v_mul_f32_e32 v7, v101, v9
	v_mul_f32_e32 v7, 0x35000000, v7
	v_med3_f32 v9, v14, s47, v197
	v_mov_b32_e32 v8, v169
	v_cvt_pk_fp8_f32 v8, v9, v11
	v_med3_f32 v11, v18, s47, v197
	v_med3_f32 v14, v19, s47, v197
	v_mov_b32_e32 v9, v169
	v_cvt_pk_fp8_f32 v9, v11, v14
	v_med3_f32 v11, v16, s47, v197
	v_med3_f32 v7, v7, s47, v197
	v_cvt_pk_fp8_f32 v8, v12, v13 op_sel:[0,0,1]
	v_cvt_pk_fp8_f32 v9, v11, v7 op_sel:[0,0,1]
	v_mad_i64_i32 v[10:11], s[22:23], v10, s46, v[4:5]
	v_lshl_add_u64 v[10:11], v[10:11], 0, v[2:3]
	global_store_dwordx2 v[10:11], v[8:9], off
	v_mul_f32_e32 v8, 0xb9b8aa3b, v94
	v_exp_f32_e32 v10, v8
	v_mul_f32_e32 v11, 0xb9b8aa3b, v95
	v_exp_f32_e32 v13, v11
	v_add_f32_e32 v10, 1.0, v10
	v_rcp_f32_e32 v10, v10
	v_add_u32_e32 v8, 0x80, v6
	v_mad_i64_i32 v[8:9], s[22:23], v8, s46, v[4:5]
	v_mul_f32_e32 v11, v94, v10
	v_add_f32_e32 v7, 1.0, v13
	v_rcp_f32_e32 v7, v7
	v_mul_f32_e32 v14, 0xb9b8aa3b, v96
	v_exp_f32_e32 v14, v14
	v_lshl_add_u64 v[8:9], v[8:9], 0, v[2:3]
	v_mul_f32_e32 v15, v90, v11
	v_mul_f32_e32 v15, 0x35000000, v15
	v_mul_f32_e32 v11, v95, v7
	v_add_f32_e32 v7, 1.0, v14
	v_mul_f32_e32 v14, 0xb9b8aa3b, v97
	v_rcp_f32_e32 v7, v7
	v_exp_f32_e32 v14, v14
	s_nop 0
	v_mul_f32_e32 v16, v91, v11
	v_mul_f32_e32 v16, 0x35000000, v16
	v_mul_f32_e32 v11, v96, v7
	v_add_f32_e32 v7, 1.0, v14
	v_rcp_f32_e32 v7, v7
	s_nop 0
	v_mul_f32_e32 v13, v92, v11
	v_mul_f32_e32 v13, 0x35000000, v13
	v_mul_f32_e32 v11, v97, v7
	v_mul_f32_e32 v10, 0xb9b8aa3b, v86
	v_exp_f32_e32 v12, v10
	v_med3_f32 v13, v13, s47, v197
	v_mul_f32_e32 v14, v93, v11
	v_mul_f32_e32 v14, 0x35000000, v14
	v_add_f32_e32 v10, 1.0, v12
	v_mul_f32_e32 v11, 0xb9b8aa3b, v87
	v_rcp_f32_e32 v10, v10
	v_exp_f32_e32 v17, v11
	v_med3_f32 v14, v14, s47, v197
	v_mul_f32_e32 v11, v86, v10
	v_add_f32_e32 v7, 1.0, v17
	v_rcp_f32_e32 v7, v7
	v_mul_f32_e32 v18, 0xb9b8aa3b, v88
	v_exp_f32_e32 v18, v18
	s_nop 0
	v_mul_f32_e32 v19, v82, v11
	v_mul_f32_e32 v19, 0x35000000, v19
	v_mul_f32_e32 v11, v87, v7
	v_add_f32_e32 v7, 1.0, v18
	v_mul_f32_e32 v18, 0xb9b8aa3b, v89
	v_rcp_f32_e32 v7, v7
	v_exp_f32_e32 v18, v18
	s_nop 0
	v_mul_f32_e32 v20, v83, v11
	v_mul_f32_e32 v20, 0x35000000, v20
	v_mul_f32_e32 v11, v88, v7
	v_add_f32_e32 v7, 1.0, v18
	v_rcp_f32_e32 v7, v7
	s_nop 0
	v_mul_f32_e32 v17, v84, v11
	v_mul_f32_e32 v17, 0x35000000, v17
	v_mul_f32_e32 v11, v89, v7
	v_med3_f32 v12, v16, s47, v197
	v_mul_f32_e32 v7, v85, v11
	v_mul_f32_e32 v7, 0x35000000, v7
	v_med3_f32 v11, v15, s47, v197
	v_mov_b32_e32 v10, v169
	v_cvt_pk_fp8_f32 v10, v11, v12
	v_med3_f32 v12, v19, s47, v197
	v_med3_f32 v15, v20, s47, v197
	v_mov_b32_e32 v11, v169
	v_cvt_pk_fp8_f32 v11, v12, v15
	v_med3_f32 v12, v17, s47, v197
	v_med3_f32 v7, v7, s47, v197
	v_cvt_pk_fp8_f32 v10, v13, v14 op_sel:[0,0,1]
	v_cvt_pk_fp8_f32 v11, v12, v7 op_sel:[0,0,1]
	v_mul_f32_e32 v12, 0xb9b8aa3b, v78
	v_exp_f32_e32 v12, v12
	global_store_dwordx2 v[8:9], v[10:11], off
	v_mul_f32_e32 v9, 0xb9b8aa3b, v79
	v_add_f32_e32 v8, 1.0, v12
	v_rcp_f32_e32 v8, v8
	v_exp_f32_e32 v12, v9
	v_add_u32_e32 v10, 0x90, v6
	v_mul_f32_e32 v9, v78, v8
	v_add_f32_e32 v7, 1.0, v12
	v_rcp_f32_e32 v7, v7
	v_mul_f32_e32 v13, 0xb9b8aa3b, v80
	v_exp_f32_e32 v13, v13
	s_nop 0
	v_mul_f32_e32 v14, v74, v9
	v_mul_f32_e32 v14, 0x35000000, v14
	v_mul_f32_e32 v9, v79, v7
	v_add_f32_e32 v7, 1.0, v13
	v_mul_f32_e32 v13, 0xb9b8aa3b, v81
	v_rcp_f32_e32 v7, v7
	v_exp_f32_e32 v13, v13
	s_nop 0
	v_mul_f32_e32 v15, v75, v9
	v_mul_f32_e32 v15, 0x35000000, v15
	v_mul_f32_e32 v9, v80, v7
	v_add_f32_e32 v7, 1.0, v13
	v_rcp_f32_e32 v7, v7
	s_nop 0
	v_mul_f32_e32 v12, v76, v9
	v_mul_f32_e32 v12, 0x35000000, v12
	v_mul_f32_e32 v9, v81, v7
	v_mul_f32_e32 v8, 0xb9b8aa3b, v70
	v_exp_f32_e32 v11, v8
	v_med3_f32 v12, v12, s47, v197
	v_mul_f32_e32 v13, v77, v9
	v_mul_f32_e32 v13, 0x35000000, v13
	v_add_f32_e32 v8, 1.0, v11
	v_mul_f32_e32 v9, 0xb9b8aa3b, v71
	v_rcp_f32_e32 v8, v8
	v_exp_f32_e32 v16, v9
	v_med3_f32 v13, v13, s47, v197
	v_mul_f32_e32 v9, v70, v8
	v_add_f32_e32 v7, 1.0, v16
	v_rcp_f32_e32 v7, v7
	v_mul_f32_e32 v17, 0xb9b8aa3b, v72
	v_exp_f32_e32 v17, v17
	s_nop 0
	v_mul_f32_e32 v18, v66, v9
	v_mul_f32_e32 v18, 0x35000000, v18
	v_mul_f32_e32 v9, v71, v7
	v_add_f32_e32 v7, 1.0, v17
	v_mul_f32_e32 v17, 0xb9b8aa3b, v73
	v_rcp_f32_e32 v7, v7
	v_exp_f32_e32 v17, v17
	s_nop 0
	v_mul_f32_e32 v19, v67, v9
	v_mul_f32_e32 v19, 0x35000000, v19
	v_mul_f32_e32 v9, v72, v7
	v_add_f32_e32 v7, 1.0, v17
	v_rcp_f32_e32 v7, v7
	s_nop 0
	v_mul_f32_e32 v16, v68, v9
	v_mul_f32_e32 v16, 0x35000000, v16
	v_mul_f32_e32 v9, v73, v7
	v_med3_f32 v11, v15, s47, v197
	v_mul_f32_e32 v7, v69, v9
	v_mul_f32_e32 v7, 0x35000000, v7
	v_med3_f32 v9, v14, s47, v197
	v_mov_b32_e32 v8, v169
	v_cvt_pk_fp8_f32 v8, v9, v11
	v_med3_f32 v11, v18, s47, v197
	v_med3_f32 v14, v19, s47, v197
	v_mov_b32_e32 v9, v169
	v_cvt_pk_fp8_f32 v9, v11, v14
	v_med3_f32 v11, v16, s47, v197
	v_med3_f32 v7, v7, s47, v197
	v_cvt_pk_fp8_f32 v8, v12, v13 op_sel:[0,0,1]
	v_cvt_pk_fp8_f32 v9, v11, v7 op_sel:[0,0,1]
	v_mad_i64_i32 v[10:11], s[22:23], v10, s46, v[4:5]
	v_lshl_add_u64 v[10:11], v[10:11], 0, v[2:3]
	global_store_dwordx2 v[10:11], v[8:9], off
	v_mul_f32_e32 v8, 0xb9b8aa3b, v62
	v_exp_f32_e32 v10, v8
	v_mul_f32_e32 v11, 0xb9b8aa3b, v63
	v_exp_f32_e32 v13, v11
	v_add_f32_e32 v10, 1.0, v10
	v_rcp_f32_e32 v10, v10
	v_add_u32_e32 v8, 0xa0, v6
	v_mad_i64_i32 v[8:9], s[22:23], v8, s46, v[4:5]
	v_mul_f32_e32 v11, v62, v10
	v_add_f32_e32 v7, 1.0, v13
	v_rcp_f32_e32 v7, v7
	v_mul_f32_e32 v14, 0xb9b8aa3b, v64
	v_exp_f32_e32 v14, v14
	v_lshl_add_u64 v[8:9], v[8:9], 0, v[2:3]
	v_mul_f32_e32 v15, v58, v11
	v_mul_f32_e32 v15, 0x35000000, v15
	v_mul_f32_e32 v11, v63, v7
	v_add_f32_e32 v7, 1.0, v14
	v_mul_f32_e32 v14, 0xb9b8aa3b, v65
	v_rcp_f32_e32 v7, v7
	v_exp_f32_e32 v14, v14
	s_nop 0
	v_mul_f32_e32 v16, v59, v11
	v_mul_f32_e32 v16, 0x35000000, v16
	v_mul_f32_e32 v11, v64, v7
	v_add_f32_e32 v7, 1.0, v14
	v_rcp_f32_e32 v7, v7
	s_nop 0
	v_mul_f32_e32 v13, v60, v11
	v_mul_f32_e32 v13, 0x35000000, v13
	v_mul_f32_e32 v11, v65, v7
	v_mul_f32_e32 v10, 0xb9b8aa3b, v54
	v_exp_f32_e32 v12, v10
	v_med3_f32 v13, v13, s47, v197
	v_mul_f32_e32 v14, v61, v11
	v_mul_f32_e32 v14, 0x35000000, v14
	v_add_f32_e32 v10, 1.0, v12
	v_mul_f32_e32 v11, 0xb9b8aa3b, v55
	v_rcp_f32_e32 v10, v10
	v_exp_f32_e32 v17, v11
	v_med3_f32 v14, v14, s47, v197
	v_mul_f32_e32 v11, v54, v10
	v_add_f32_e32 v7, 1.0, v17
	v_rcp_f32_e32 v7, v7
	v_mul_f32_e32 v18, 0xb9b8aa3b, v56
	v_exp_f32_e32 v18, v18
	s_nop 0
	v_mul_f32_e32 v19, v50, v11
	v_mul_f32_e32 v19, 0x35000000, v19
	v_mul_f32_e32 v11, v55, v7
	v_add_f32_e32 v7, 1.0, v18
	v_mul_f32_e32 v18, 0xb9b8aa3b, v57
	v_rcp_f32_e32 v7, v7
	v_exp_f32_e32 v18, v18
	s_nop 0
	v_mul_f32_e32 v20, v51, v11
	v_mul_f32_e32 v20, 0x35000000, v20
	v_mul_f32_e32 v11, v56, v7
	v_add_f32_e32 v7, 1.0, v18
	v_rcp_f32_e32 v7, v7
	s_nop 0
	v_mul_f32_e32 v17, v52, v11
	v_mul_f32_e32 v17, 0x35000000, v17
	v_mul_f32_e32 v11, v57, v7
	v_med3_f32 v12, v16, s47, v197
	v_mul_f32_e32 v7, v53, v11
	v_mul_f32_e32 v7, 0x35000000, v7
	v_med3_f32 v11, v15, s47, v197
	v_mov_b32_e32 v10, v169
	v_cvt_pk_fp8_f32 v10, v11, v12
	v_med3_f32 v12, v19, s47, v197
	v_med3_f32 v15, v20, s47, v197
	v_mov_b32_e32 v11, v169
	v_cvt_pk_fp8_f32 v11, v12, v15
	v_med3_f32 v12, v17, s47, v197
	v_med3_f32 v7, v7, s47, v197
	v_cvt_pk_fp8_f32 v10, v13, v14 op_sel:[0,0,1]
	v_cvt_pk_fp8_f32 v11, v12, v7 op_sel:[0,0,1]
	v_mul_f32_e32 v12, 0xb9b8aa3b, v46
	v_exp_f32_e32 v12, v12
	global_store_dwordx2 v[8:9], v[10:11], off
	v_mul_f32_e32 v10, 0xb9b8aa3b, v47
	v_exp_f32_e32 v10, v10
	v_add_u32_e32 v8, 0xb0, v6
	v_add_f32_e32 v6, 1.0, v12
	v_rcp_f32_e32 v6, v6
	v_add_f32_e32 v10, 1.0, v10
	v_rcp_f32_e32 v10, v10
	v_mul_f32_e32 v12, 0xb9b8aa3b, v48
	v_exp_f32_e32 v12, v12
	v_mul_f32_e32 v7, v46, v6
	v_mad_i64_i32 v[4:5], s[22:23], v8, s46, v[4:5]
	v_mul_f32_e32 v13, v42, v7
	v_mul_f32_e32 v13, 0x35000000, v13
	v_mul_f32_e32 v7, v47, v10
	v_add_f32_e32 v9, 1.0, v12
	v_mul_f32_e32 v12, 0xb9b8aa3b, v49
	v_exp_f32_e32 v12, v12
	v_rcp_f32_e32 v9, v9
	v_lshl_add_u64 v[2:3], v[4:5], 0, v[2:3]
	v_mul_f32_e32 v14, v43, v7
	v_mul_f32_e32 v14, 0x35000000, v14
	v_add_f32_e32 v6, 1.0, v12
	v_mul_f32_e32 v7, v48, v9
	v_rcp_f32_e32 v9, v6
	s_nop 0
	v_mul_f32_e32 v11, v44, v7
	v_mul_f32_e32 v11, 0x35000000, v11
	v_mul_f32_e32 v7, v49, v9
	v_mul_f32_e32 v6, 0xb9b8aa3b, v38
	v_exp_f32_e32 v10, v6
	v_med3_f32 v11, v11, s47, v197
	v_mul_f32_e32 v12, v45, v7
	v_mul_f32_e32 v12, 0x35000000, v12
	v_add_f32_e32 v6, 1.0, v10
	v_mul_f32_e32 v7, 0xb9b8aa3b, v39
	v_rcp_f32_e32 v6, v6
	v_exp_f32_e32 v15, v7
	v_med3_f32 v12, v12, s47, v197
	v_mul_f32_e32 v7, v38, v6
	v_add_f32_e32 v9, 1.0, v15
	v_rcp_f32_e32 v9, v9
	v_mul_f32_e32 v16, 0xb9b8aa3b, v40
	v_exp_f32_e32 v16, v16
	s_nop 0
	v_mul_f32_e32 v17, v34, v7
	v_mul_f32_e32 v17, 0x35000000, v17
	v_mul_f32_e32 v7, v39, v9
	v_add_f32_e32 v9, 1.0, v16
	v_mul_f32_e32 v16, 0xb9b8aa3b, v41
	v_exp_f32_e32 v16, v16
	v_rcp_f32_e32 v9, v9
	s_nop 0
	v_mul_f32_e32 v18, v35, v7
	v_mul_f32_e32 v18, 0x35000000, v18
	v_add_f32_e32 v6, 1.0, v16
	v_mul_f32_e32 v7, v40, v9
	v_rcp_f32_e32 v9, v6
	s_nop 0
	v_mul_f32_e32 v15, v36, v7
	v_mul_f32_e32 v15, 0x35000000, v15
	v_mul_f32_e32 v7, v41, v9
	v_med3_f32 v10, v14, s47, v197
	v_mul_f32_e32 v9, v37, v7
	v_mul_f32_e32 v9, 0x35000000, v9
	v_med3_f32 v7, v13, s47, v197
	v_mov_b32_e32 v6, v169
	v_cvt_pk_fp8_f32 v6, v7, v10
	v_med3_f32 v10, v17, s47, v197
	v_med3_f32 v13, v18, s47, v197
	v_mov_b32_e32 v7, v169
	v_cvt_pk_fp8_f32 v7, v10, v13
	v_med3_f32 v10, v15, s47, v197
	v_med3_f32 v9, v9, s47, v197
	v_cvt_pk_fp8_f32 v6, v11, v12 op_sel:[0,0,1]
	v_cvt_pk_fp8_f32 v7, v10, v9 op_sel:[0,0,1]
	global_store_dwordx2 v[2:3], v[6:7], off
	s_cbranch_vccnz .LBB0_1953
	s_andn2_b64 vcc, exec, s[6:7]
	s_cbranch_vccnz .LBB0_1952
	s_barrier
	s_branch .LBB0_1952
